# MoE: counted vmcnt kept in K loop; MoE1 row-list loads issued together; MoE2 epilogue stores paired to dwordx4 via permlane16_swap
# speedup vs baseline: 1.0657x; 1.0002x over previous
.LBB0_3322:
	s_mov_b32 s9, s65
	s_lshl_b64 s[0:1], s[8:9], 2
	v_mov_b32_e32 v2, v0
	s_add_u32 s12, s47, s0
	s_addc_u32 s13, s48, s1
	v_readfirstlane_b32 s15, v2
	s_sub_i32 s9, s46, s8
	s_ashr_i32 s14, s15, 6
	v_bfe_u32 v231, v2, 4, 2
	s_min_i32 s9, s9, 0x280
	v_bitop3_b32 v3, v231, v2, 3 bitop3:0x78
	v_bfe_u32 v8, v2, 2, 4
	s_mul_i32 s16, s14, 0x50
	s_add_i32 s11, s9, -1
	v_lshlrev_b32_e32 v86, 4, v3
	v_or_b32_e32 v3, s16, v8
	v_min_i32_e32 v202, s11, v3
	v_ashrrev_i32_e32 v203, 31, v202
	v_lshl_add_u64 v[202:203], v[202:203], 2, s[12:13]
	global_load_dword v202, v[202:203], off
	s_add_i32 s17, s16, 16
	v_lshl_add_u64 v[4:5], s[2:3], 0, v[86:87]
	v_or_b32_e32 v3, s17, v8
	s_add_i32 s17, s16, 32


	v_min_i32_e32 v204, s11, v3
	v_ashrrev_i32_e32 v205, 31, v204
	v_lshl_add_u64 v[204:205], v[204:205], 2, s[12:13]
	global_load_dword v204, v[204:205], off
	v_or_b32_e32 v3, s17, v8
	s_add_i32 s17, s16, 48
	s_add_i32 s16, s16, 64


	v_min_i32_e32 v206, s11, v3
	v_ashrrev_i32_e32 v207, 31, v206
	v_lshl_add_u64 v[206:207], v[206:207], 2, s[12:13]
	global_load_dword v206, v[206:207], off
	v_or_b32_e32 v3, s17, v8


	v_min_i32_e32 v208, s11, v3
	v_ashrrev_i32_e32 v209, 31, v208
	v_lshl_add_u64 v[208:209], v[208:209], 2, s[12:13]
	global_load_dword v208, v[208:209], off
	v_or_b32_e32 v3, s16, v8
	s_mov_b64 s[16:17], -1


	v_min_i32_e32 v210, s11, v3
	v_ashrrev_i32_e32 v211, 31, v210
	v_lshl_add_u64 v[210:211], v[210:211], 2, s[12:13]
	global_load_dword v210, v[210:211], off
	s_mov_b32 s11, s65
	v_ashrrev_i32_e32 v3, 5, v2
	v_lshlrev_b32_e32 v8, 1, v3
	v_ashrrev_i32_e32 v9, 31, v8
	v_lshlrev_b64 v[8:9], 11, v[8:9]
	s_add_i32 s12, s9, 63
	s_lshr_b32 s13, s12, 2
	s_and_b32 s13, s13, 0x3ffffff0
	s_lshr_b32 s12, s12, 6
	s_add_i32 s12, s12, 1
	s_lshr_b32 s19, s12, 1
	s_waitcnt vmcnt(0)
	v_ashrrev_i32_e32 v203, 31, v202
	v_lshlrev_b64 v[202:203], 12, v[202:203]
	v_lshl_add_u64 v[202:203], v[4:5], 0, v[202:203]
	v_ashrrev_i32_e32 v205, 31, v204
	v_lshlrev_b64 v[204:205], 12, v[204:205]
	v_lshl_add_u64 v[204:205], v[4:5], 0, v[204:205]
	v_ashrrev_i32_e32 v207, 31, v206
	v_lshlrev_b64 v[206:207], 12, v[206:207]
	v_lshl_add_u64 v[206:207], v[4:5], 0, v[206:207]
	v_ashrrev_i32_e32 v209, 31, v208
	v_lshlrev_b64 v[208:209], 12, v[208:209]
	v_lshl_add_u64 v[208:209], v[4:5], 0, v[208:209]
	v_ashrrev_i32_e32 v211, 31, v210
	v_lshlrev_b64 v[210:211], 12, v[210:211]
	v_lshl_add_u64 v[210:211], v[4:5], 0, v[210:211]


	v_and_b32_e32 v5, 8, v2
	v_cmp_eq_u32_e32 vcc, 0, v5
	v_mov_b32_e32 v5, s36
	v_mov_b32_e32 v6, s34
	v_cndmask_b32_e32 v7, v5, v6, vcc
	v_mov_b32_e32 v5, s37
	v_mov_b32_e32 v6, s35
	v_cndmask_b32_e32 v6, v5, v6, vcc
	v_lshl_add_u64 v[6:7], s[4:5], 2, v[6:7]
	v_lshl_add_u64 v[6:7], v[6:7], 0, s[6:7]
	v_lshl_add_u64 v[6:7], v[6:7], 0, s[10:11]
	s_mul_i32 s11, s14, 0x1400
	s_add_i32 s18, s11, 0
	s_mov_b32 m0, s18
	v_lshlrev_b32_e32 v5, 3, v2
	global_load_lds_dwordx4 v[202:203], off
	s_add_i32 m0, s18, 0x400
	v_and_b32_e32 v86, 0x80, v5
	v_lshlrev_b32_e32 v5, 4, v2
	global_load_lds_dwordx4 v[204:205], off
	s_add_i32 m0, s18, 0x800
	v_lshl_add_u64 v[6:7], v[6:7], 0, v[86:87]
	v_and_b32_e32 v86, 0x70, v5
	global_load_lds_dwordx4 v[206:207], off
	s_add_i32 m0, s18, 0xc00
	v_lshl_add_u64 v[6:7], v[6:7], 0, v[86:87]
	global_load_lds_dwordx4 v[208:209], off
	s_add_i32 m0, s18, 0x1000
	v_lshl_add_u64 v[212:213], v[6:7], 0, v[8:9]
	global_load_lds_dwordx4 v[210:211], off
	v_lshl_add_u64 v[6:7], v[202:203], 0, 64
	s_add_i32 m0, s18, 0xa000
	global_load_dwordx4 v[74:77], v[212:213], off nt
	global_load_dwordx4 v[78:81], v[212:213], off offset:2048 nt
	v_and_b32_e32 v4, 31, v2
	global_load_lds_dwordx4 v[6:7], off
	v_lshl_add_u64 v[6:7], v[204:205], 0, 64
	s_add_i32 m0, s18, 0xa400
	s_ashr_i32 s11, s15, 7
	global_load_lds_dwordx4 v[6:7], off
	v_lshl_add_u64 v[6:7], v[206:207], 0, 64
	s_add_i32 m0, s18, 0xa800
	v_and_b32_e32 v5, 15, v2
	global_load_lds_dwordx4 v[6:7], off
	v_lshl_add_u64 v[6:7], v[208:209], 0, 64
	s_add_i32 m0, s18, 0xac00
	v_lshrrev_b32_e32 v2, 2, v2
	global_load_lds_dwordx4 v[6:7], off
	v_lshl_add_u64 v[6:7], v[210:211], 0, 64
	s_add_i32 m0, s18, 0xb000
	s_mul_i32 s13, s13, s11
	global_load_lds_dwordx4 v[6:7], off
	v_add_co_u32_e32 v6, vcc, 0x10000, v212
	v_bitop3_b32 v2, v231, v2, 3 bitop3:0x78
	s_nop 0
	v_addc_co_u32_e32 v7, vcc, 0, v213, vcc
	global_load_dwordx4 v[30:33], v[6:7], off nt
	global_load_dwordx4 v[34:37], v[6:7], off offset:2048 nt
	v_or_b32_e32 v200, s13, v5
	v_lshlrev_b32_e32 v2, 4, v2
	v_lshl_or_b32 v86, v200, 6, v2
	v_mul_u32_u24_e32 v2, 0x840, v231
	s_and_b32 s11, s14, 1
	s_movk_i32 s13, 0x210
	v_lshl_or_b32 v2, v5, 2, v2
	v_mul_lo_u32 v3, v3, s13
	v_lshl_add_u32 v2, s11, 8, v2
	v_lshl_add_u32 v164, v4, 4, v3
	v_add_u32_e32 v201, 0x1e000, v2
	v_add_u32_e32 v232, 0x1e420, v2
	v_add_u32_e32 v233, 0x20100, v2
	v_add_u32_e32 v234, 0x20520, v2
	s_mov_b64 s[12:13], 0
	s_cmp_lt_i32 s19, 3
	s_mov_b64 s[14:15], 0
	s_cbranch_scc1 .LBB0_3334
	s_cmp_gt_i32 s19, 3
	s_cbranch_scc0 .LBB0_3328
	s_cmp_eq_u32 s19, 4
	s_mov_b64 s[14:15], -1
	s_cbranch_scc0 .LBB0_3329
	s_waitcnt vmcnt(7)
	v_add_u32_e32 v165, 0, v164
	s_waitcnt vmcnt(0)
	v_cvt_pk_bf16_f32 v2, v74, v78
	v_cvt_pk_bf16_f32 v3, v75, v79
	v_cvt_pk_bf16_f32 v4, v76, v80
	v_cvt_pk_bf16_f32 v5, v77, v81
	v_add_u32_e32 v166, 0x1e000, v165
	v_mov_b32_e32 v70, 0
	v_mov_b64_e32 v[150:151], v[36:37]
	v_mov_b64_e32 v[154:155], v[32:33]
	ds_write_b128 v166, v[2:5]
	s_mov_b32 s14, 0
	s_mov_b32 s16, -2
	v_mov_b64_e32 v[148:149], v[34:35]
	v_mov_b64_e32 v[152:153], v[30:31]
	v_mov_b32_e32 v71, v70
	v_mov_b32_e32 v72, v70
	v_mov_b32_e32 v73, v70
	v_mov_b32_e32 v50, v70
	v_mov_b32_e32 v51, v70
	v_mov_b32_e32 v52, v70
	v_mov_b32_e32 v53, v70
	v_mov_b32_e32 v10, v70
	v_mov_b32_e32 v11, v70
	v_mov_b32_e32 v12, v70
	v_mov_b32_e32 v13, v70
	v_mov_b32_e32 v2, v70
	v_mov_b32_e32 v3, v70
	v_mov_b32_e32 v4, v70
	v_mov_b32_e32 v5, v70
	v_mov_b32_e32 v104, v70
	v_mov_b32_e32 v105, v70
	v_mov_b32_e32 v106, v70
	v_mov_b32_e32 v107, v70
	v_mov_b32_e32 v120, v70
	v_mov_b32_e32 v121, v70
	v_mov_b32_e32 v122, v70
	v_mov_b32_e32 v123, v70
	v_mov_b32_e32 v100, v70
	v_mov_b32_e32 v101, v70
	v_mov_b32_e32 v102, v70
	v_mov_b32_e32 v103, v70
	v_mov_b32_e32 v108, v70
	v_mov_b32_e32 v109, v70
	v_mov_b32_e32 v110, v70
	v_mov_b32_e32 v111, v70
	v_mov_b32_e32 v38, v70
	v_mov_b32_e32 v39, v70
	v_mov_b32_e32 v40, v70
	v_mov_b32_e32 v41, v70
	v_mov_b32_e32 v18, v70
	v_mov_b32_e32 v19, v70
	v_mov_b32_e32 v20, v70
	v_mov_b32_e32 v21, v70
	v_mov_b32_e32 v46, v70
	v_mov_b32_e32 v47, v70
	v_mov_b32_e32 v48, v70
	v_mov_b32_e32 v49, v70
	v_mov_b32_e32 v22, v70
	v_mov_b32_e32 v23, v70
	v_mov_b32_e32 v24, v70
	v_mov_b32_e32 v25, v70
	v_mov_b32_e32 v66, v70
	v_mov_b32_e32 v67, v70
	v_mov_b32_e32 v68, v70
	v_mov_b32_e32 v69, v70
	v_mov_b32_e32 v96, v70
	v_mov_b32_e32 v97, v70
	v_mov_b32_e32 v98, v70
	v_mov_b32_e32 v99, v70
	v_mov_b32_e32 v62, v70
	v_mov_b32_e32 v63, v70
	v_mov_b32_e32 v64, v70
	v_mov_b32_e32 v65, v70
	v_mov_b32_e32 v92, v70
	v_mov_b32_e32 v93, v70
	v_mov_b32_e32 v94, v70
	v_mov_b32_e32 v95, v70
	v_mov_b32_e32 v26, v70
	v_mov_b32_e32 v27, v70
	v_mov_b32_e32 v28, v70
	v_mov_b32_e32 v29, v70
	v_mov_b32_e32 v6, v70
	v_mov_b32_e32 v7, v70
	v_mov_b32_e32 v8, v70
	v_mov_b32_e32 v9, v70
	v_mov_b32_e32 v42, v70
	v_mov_b32_e32 v43, v70
	v_mov_b32_e32 v44, v70
	v_mov_b32_e32 v45, v70
	v_mov_b32_e32 v14, v70
	v_mov_b32_e32 v15, v70
	v_mov_b32_e32 v16, v70
	v_mov_b32_e32 v17, v70
	v_mov_b32_e32 v58, v70
	v_mov_b32_e32 v59, v70
	v_mov_b32_e32 v60, v70
	v_mov_b32_e32 v61, v70
	v_mov_b32_e32 v88, v70
	v_mov_b32_e32 v89, v70
	v_mov_b32_e32 v90, v70
	v_mov_b32_e32 v91, v70
	v_mov_b32_e32 v54, v70
	v_mov_b32_e32 v55, v70
	v_mov_b32_e32 v56, v70
	v_mov_b32_e32 v57, v70
	v_mov_b32_e32 v82, v70
	v_mov_b32_e32 v83, v70
	v_mov_b32_e32 v84, v70
	v_mov_b32_e32 v85, v70
	v_mov_b32_e32 v124, v70
	v_mov_b32_e32 v125, v70
	v_mov_b32_e32 v126, v70
	v_mov_b32_e32 v127, v70
	v_mov_b32_e32 v112, v70
	v_mov_b32_e32 v113, v70
	v_mov_b32_e32 v114, v70
	v_mov_b32_e32 v115, v70
	v_mov_b32_e32 v128, v70
	v_mov_b32_e32 v129, v70
	v_mov_b32_e32 v130, v70
	v_mov_b32_e32 v131, v70
	v_mov_b32_e32 v116, v70
	v_mov_b32_e32 v117, v70
	v_mov_b32_e32 v118, v70
	v_mov_b32_e32 v119, v70
	v_mov_b32_e32 v140, v70
	v_mov_b32_e32 v141, v70
	v_mov_b32_e32 v142, v70
	v_mov_b32_e32 v143, v70
	v_mov_b32_e32 v132, v70
	v_mov_b32_e32 v133, v70
	v_mov_b32_e32 v134, v70
	v_mov_b32_e32 v135, v70
	v_mov_b32_e32 v144, v70
	v_mov_b32_e32 v145, v70
	v_mov_b32_e32 v146, v70
	v_mov_b32_e32 v147, v70
	v_mov_b32_e32 v136, v70
	v_mov_b32_e32 v137, v70
	v_mov_b32_e32 v138, v70
	v_mov_b32_e32 v139, v70

.LBB0_3472:
	s_lshl_b32 s4, s21, 1
	s_add_u32 s4, s17, s4
	s_addc_u32 s5, s18, 0
	v_lshlrev_b32_e32 v86, 3, v231
	v_and_b32_e32 v180, 1, v231
	v_mul_u32_u24_e32 v180, 24, v180
	v_add_u32_e32 v86, v86, v180
	s_waitcnt vmcnt(0)
	v_lshl_add_u64 v[2:3], s[4:5], 0, v[86:87]
	v_cmp_gt_i32_e32 vcc, s20, v213
	s_and_saveexec_b64 s[4:5], vcc
	s_cbranch_execz .LBB0_3474
	v_add_u32_e32 v4, v213, v212
	v_ashrrev_i32_e32 v5, 31, v4
	v_lshlrev_b64 v[4:5], 12, v[4:5]
	v_lshl_add_u64 v[4:5], v[2:3], 0, v[4:5]
	v_cvt_pk_bf16_f32 v180, v78, v79
	v_cvt_pk_bf16_f32 v181, v80, v81
	v_cvt_pk_bf16_f32 v182, v74, v75
	v_cvt_pk_bf16_f32 v183, v76, v77
	v_cvt_pk_bf16_f32 v184, v70, v71
	v_cvt_pk_bf16_f32 v185, v72, v73
	v_cvt_pk_bf16_f32 v186, v66, v67
	v_cvt_pk_bf16_f32 v187, v68, v69
	s_nop 1
	v_permlane16_swap_b32_e32 v180, v182
	v_permlane16_swap_b32_e32 v181, v183
	v_permlane16_swap_b32_e32 v184, v186
	v_permlane16_swap_b32_e32 v185, v187
	global_store_dwordx4 v[4:5], v[180:183], off
	global_store_dwordx4 v[4:5], v[184:187], off offset:64


.LBB0_3474:
	s_or_b64 exec, exec, s[4:5]
	s_cmp_gt_u32 s20, 64
	v_add_u32_e32 v4, 16, v213
	s_cselect_b64 s[4:5], -1, 0
	v_cmp_gt_i32_e32 vcc, s20, v4
	s_and_b64 s[6:7], s[4:5], vcc
	s_and_saveexec_b64 s[4:5], s[6:7]
	s_cbranch_execz .LBB0_3476
	v_add_u32_e32 v4, v4, v212
	v_ashrrev_i32_e32 v5, 31, v4
	v_lshlrev_b64 v[4:5], 12, v[4:5]
	v_lshl_add_u64 v[4:5], v[2:3], 0, v[4:5]
	v_cvt_pk_bf16_f32 v180, v62, v63
	v_cvt_pk_bf16_f32 v181, v64, v65
	v_cvt_pk_bf16_f32 v182, v58, v59
	v_cvt_pk_bf16_f32 v183, v60, v61
	v_cvt_pk_bf16_f32 v184, v54, v55
	v_cvt_pk_bf16_f32 v185, v56, v57
	v_cvt_pk_bf16_f32 v186, v50, v51
	v_cvt_pk_bf16_f32 v187, v52, v53
	s_nop 1
	v_permlane16_swap_b32_e32 v180, v182
	v_permlane16_swap_b32_e32 v181, v183
	v_permlane16_swap_b32_e32 v184, v186
	v_permlane16_swap_b32_e32 v185, v187
	global_store_dwordx4 v[4:5], v[180:183], off
	global_store_dwordx4 v[4:5], v[184:187], off offset:64


.LBB0_3476:
	s_or_b64 exec, exec, s[4:5]
	s_cmpk_gt_u32 s20, 0x80
	v_add_u32_e32 v4, 32, v213
	s_cselect_b64 s[4:5], -1, 0
	v_cmp_gt_i32_e32 vcc, s20, v4
	s_and_b64 s[6:7], s[4:5], vcc
	s_and_saveexec_b64 s[4:5], s[6:7]
	s_cbranch_execz .LBB0_3478
	v_add_u32_e32 v4, v4, v212
	v_ashrrev_i32_e32 v5, 31, v4
	v_lshlrev_b64 v[4:5], 12, v[4:5]
	v_lshl_add_u64 v[4:5], v[2:3], 0, v[4:5]
	v_cvt_pk_bf16_f32 v180, v46, v47
	v_cvt_pk_bf16_f32 v181, v48, v49
	v_cvt_pk_bf16_f32 v182, v42, v43
	v_cvt_pk_bf16_f32 v183, v44, v45
	v_cvt_pk_bf16_f32 v184, v38, v39
	v_cvt_pk_bf16_f32 v185, v40, v41
	v_cvt_pk_bf16_f32 v186, v34, v35
	v_cvt_pk_bf16_f32 v187, v36, v37
	s_nop 1
	v_permlane16_swap_b32_e32 v180, v182
	v_permlane16_swap_b32_e32 v181, v183
	v_permlane16_swap_b32_e32 v184, v186
	v_permlane16_swap_b32_e32 v185, v187
	global_store_dwordx4 v[4:5], v[180:183], off
	global_store_dwordx4 v[4:5], v[184:187], off offset:64


.LBB0_3478:
	s_or_b64 exec, exec, s[4:5]
	s_cmpk_gt_u32 s20, 0xc0
	v_add_u32_e32 v4, 48, v213
	s_cselect_b64 s[4:5], -1, 0
	v_cmp_gt_i32_e32 vcc, s20, v4
	s_and_b64 s[6:7], s[4:5], vcc
	s_and_saveexec_b64 s[4:5], s[6:7]
	s_cbranch_execz .LBB0_3480
	v_add_u32_e32 v4, v4, v212
	v_ashrrev_i32_e32 v5, 31, v4
	v_lshlrev_b64 v[4:5], 12, v[4:5]
	v_lshl_add_u64 v[4:5], v[2:3], 0, v[4:5]
	v_cvt_pk_bf16_f32 v180, v18, v19
	v_cvt_pk_bf16_f32 v181, v20, v21
	v_cvt_pk_bf16_f32 v182, v22, v23
	v_cvt_pk_bf16_f32 v183, v24, v25
	v_cvt_pk_bf16_f32 v184, v26, v27
	v_cvt_pk_bf16_f32 v185, v28, v29
	v_cvt_pk_bf16_f32 v186, v30, v31
	v_cvt_pk_bf16_f32 v187, v32, v33
	s_nop 1
	v_permlane16_swap_b32_e32 v180, v182
	v_permlane16_swap_b32_e32 v181, v183
	v_permlane16_swap_b32_e32 v184, v186
	v_permlane16_swap_b32_e32 v185, v187
	global_store_dwordx4 v[4:5], v[180:183], off
	global_store_dwordx4 v[4:5], v[184:187], off offset:64


.LBB0_3480:
	s_or_b64 exec, exec, s[4:5]
	s_cmpk_gt_u32 s20, 0x100
	v_add_u32_e32 v4, 64, v213
	s_cselect_b64 s[4:5], -1, 0
	v_cmp_gt_i32_e32 vcc, s20, v4
	s_and_b64 s[6:7], s[4:5], vcc
	s_and_saveexec_b64 s[4:5], s[6:7]
	s_cbranch_execz .LBB0_3482
	v_add_u32_e32 v4, v4, v212
	v_ashrrev_i32_e32 v5, 31, v4
	v_lshlrev_b64 v[4:5], 12, v[4:5]
	v_lshl_add_u64 v[4:5], v[2:3], 0, v[4:5]
	v_cvt_pk_bf16_f32 v180, v88, v89
	v_cvt_pk_bf16_f32 v181, v90, v91
	v_cvt_pk_bf16_f32 v182, v112, v113
	v_cvt_pk_bf16_f32 v183, v114, v115
	v_cvt_pk_bf16_f32 v184, v108, v109
	v_cvt_pk_bf16_f32 v185, v110, v111
	v_cvt_pk_bf16_f32 v186, v100, v101
	v_cvt_pk_bf16_f32 v187, v102, v103
	s_nop 1
	v_permlane16_swap_b32_e32 v180, v182
	v_permlane16_swap_b32_e32 v181, v183
	v_permlane16_swap_b32_e32 v184, v186
	v_permlane16_swap_b32_e32 v185, v187
	global_store_dwordx4 v[4:5], v[180:183], off
	global_store_dwordx4 v[4:5], v[184:187], off offset:64


.LBB0_3482:
	s_or_b64 exec, exec, s[4:5]
	s_cmpk_gt_u32 s20, 0x140
	v_add_u32_e32 v4, 0x50, v213
	s_cselect_b64 s[4:5], -1, 0
	v_cmp_gt_i32_e32 vcc, s20, v4
	s_and_b64 s[6:7], s[4:5], vcc
	s_and_saveexec_b64 s[4:5], s[6:7]
	s_cbranch_execz .LBB0_3484
	v_add_u32_e32 v4, v4, v212
	v_ashrrev_i32_e32 v5, 31, v4
	v_lshlrev_b64 v[4:5], 12, v[4:5]
	v_lshl_add_u64 v[4:5], v[2:3], 0, v[4:5]
	v_cvt_pk_bf16_f32 v180, v82, v83
	v_cvt_pk_bf16_f32 v181, v84, v85
	v_cvt_pk_bf16_f32 v182, v92, v93
	v_cvt_pk_bf16_f32 v183, v94, v95
	v_cvt_pk_bf16_f32 v184, v96, v97
	v_cvt_pk_bf16_f32 v185, v98, v99
	v_cvt_pk_bf16_f32 v186, v104, v105
	v_cvt_pk_bf16_f32 v187, v106, v107
	s_nop 1
	v_permlane16_swap_b32_e32 v180, v182
	v_permlane16_swap_b32_e32 v181, v183
	v_permlane16_swap_b32_e32 v184, v186
	v_permlane16_swap_b32_e32 v185, v187
	global_store_dwordx4 v[4:5], v[180:183], off
	global_store_dwordx4 v[4:5], v[184:187], off offset:64


.LBB0_3484:
	s_or_b64 exec, exec, s[4:5]
	s_cmpk_gt_u32 s20, 0x180
	v_add_u32_e32 v4, 0x60, v213
	s_cselect_b64 s[4:5], -1, 0
	v_cmp_gt_i32_e32 vcc, s20, v4
	s_and_b64 s[6:7], s[4:5], vcc
	s_and_saveexec_b64 s[4:5], s[6:7]
	s_cbranch_execz .LBB0_3486
	v_add_u32_e32 v4, v4, v212
	v_ashrrev_i32_e32 v5, 31, v4
	v_lshlrev_b64 v[4:5], 12, v[4:5]
	v_lshl_add_u64 v[4:5], v[2:3], 0, v[4:5]
	v_cvt_pk_bf16_f32 v180, v116, v117
	v_cvt_pk_bf16_f32 v181, v118, v119
	v_cvt_pk_bf16_f32 v182, v124, v125
	v_cvt_pk_bf16_f32 v183, v126, v127
	v_cvt_pk_bf16_f32 v184, v132, v133
	v_cvt_pk_bf16_f32 v185, v134, v135
	v_cvt_pk_bf16_f32 v186, v136, v137
	v_cvt_pk_bf16_f32 v187, v138, v139
	s_nop 1
	v_permlane16_swap_b32_e32 v180, v182
	v_permlane16_swap_b32_e32 v181, v183
	v_permlane16_swap_b32_e32 v184, v186
	v_permlane16_swap_b32_e32 v185, v187
	global_store_dwordx4 v[4:5], v[180:183], off
	global_store_dwordx4 v[4:5], v[184:187], off offset:64


.LBB0_3486:
	s_or_b64 exec, exec, s[4:5]
	s_cmpk_gt_u32 s20, 0x1c0
	v_add_u32_e32 v4, 0x70, v213
	s_cselect_b64 s[4:5], -1, 0
	v_cmp_gt_i32_e32 vcc, s20, v4
	s_and_b64 s[6:7], s[4:5], vcc
	s_and_saveexec_b64 s[4:5], s[6:7]
	s_cbranch_execz .LBB0_3488
	v_add_u32_e32 v4, v4, v212
	v_ashrrev_i32_e32 v5, 31, v4
	v_lshlrev_b64 v[4:5], 12, v[4:5]
	v_lshl_add_u64 v[4:5], v[2:3], 0, v[4:5]
	v_cvt_pk_bf16_f32 v180, v120, v121
	v_cvt_pk_bf16_f32 v181, v122, v123
	v_cvt_pk_bf16_f32 v182, v128, v129
	v_cvt_pk_bf16_f32 v183, v130, v131
	v_cvt_pk_bf16_f32 v184, v140, v141
	v_cvt_pk_bf16_f32 v185, v142, v143
	v_cvt_pk_bf16_f32 v186, v144, v145
	v_cvt_pk_bf16_f32 v187, v146, v147
	s_nop 1
	v_permlane16_swap_b32_e32 v180, v182
	v_permlane16_swap_b32_e32 v181, v183
	v_permlane16_swap_b32_e32 v184, v186
	v_permlane16_swap_b32_e32 v185, v187
	global_store_dwordx4 v[4:5], v[180:183], off
	global_store_dwordx4 v[4:5], v[184:187], off offset:64


.LBB0_3488:
	s_or_b64 exec, exec, s[4:5]
	s_cmpk_gt_u32 s20, 0x200
	v_add_u32_e32 v4, 0x80, v213
	s_cselect_b64 s[4:5], -1, 0
	v_cmp_gt_i32_e32 vcc, s20, v4
	s_and_b64 s[6:7], s[4:5], vcc
	s_and_saveexec_b64 s[4:5], s[6:7]
	s_cbranch_execz .LBB0_3490
	v_add_u32_e32 v4, v4, v212
	v_ashrrev_i32_e32 v5, 31, v4
	v_lshlrev_b64 v[4:5], 12, v[4:5]
	v_lshl_add_u64 v[4:5], v[2:3], 0, v[4:5]
	v_cvt_pk_bf16_f32 v180, v148, v149
	v_cvt_pk_bf16_f32 v181, v150, v151
	v_cvt_pk_bf16_f32 v182, v176, v177
	v_cvt_pk_bf16_f32 v183, v178, v179
	v_cvt_pk_bf16_f32 v184, v172, v173
	v_cvt_pk_bf16_f32 v185, v174, v175
	v_cvt_pk_bf16_f32 v186, v168, v169
	v_cvt_pk_bf16_f32 v187, v170, v171
	s_nop 1
	v_permlane16_swap_b32_e32 v180, v182
	v_permlane16_swap_b32_e32 v181, v183
	v_permlane16_swap_b32_e32 v184, v186
	v_permlane16_swap_b32_e32 v185, v187
	global_store_dwordx4 v[4:5], v[180:183], off
	global_store_dwordx4 v[4:5], v[184:187], off offset:64


.LBB0_3490:
	s_or_b64 exec, exec, s[4:5]
	s_cmpk_gt_u32 s20, 0x240
	v_add_u32_e32 v4, 0x90, v213
	s_cselect_b64 s[4:5], -1, 0
	v_cmp_gt_i32_e32 vcc, s20, v4
	s_and_b64 s[6:7], s[4:5], vcc
	s_and_saveexec_b64 s[4:5], s[6:7]
	s_cbranch_execz .LBB0_3443
	v_add_u32_e32 v4, v4, v212
	v_ashrrev_i32_e32 v5, 31, v4
	v_lshlrev_b64 v[4:5], 12, v[4:5]
	v_lshl_add_u64 v[2:3], v[2:3], 0, v[4:5]
	v_cvt_pk_bf16_f32 v180, v164, v165
	v_cvt_pk_bf16_f32 v181, v166, v167
	v_cvt_pk_bf16_f32 v182, v160, v161
	v_cvt_pk_bf16_f32 v183, v162, v163
	v_cvt_pk_bf16_f32 v184, v156, v157
	v_cvt_pk_bf16_f32 v185, v158, v159
	v_cvt_pk_bf16_f32 v186, v152, v153
	v_cvt_pk_bf16_f32 v187, v154, v155
	s_nop 1
	v_permlane16_swap_b32_e32 v180, v182
	v_permlane16_swap_b32_e32 v181, v183
	v_permlane16_swap_b32_e32 v184, v186
	v_permlane16_swap_b32_e32 v185, v187
	global_store_dwordx4 v[2:3], v[180:183], off
	global_store_dwordx4 v[2:3], v[184:187], off offset:64


	s_branch .LBB0_3443
